# v61 + layer-0 out-projection epilogue with twelve residual-load steps in flight
# speedup vs baseline: 1.0040x; 1.0023x over previous
; __device__ __forceinline__ u32x4 pack8(const f32x4 v0, const f32x4 v1) { u32x4 w; w.x = cvt_pk_bf16(v0[0], v0[1]); w.y = cvt_pk_bf16(v0[2], v0[3]); w.z = cvt_pk_bf16(v1[0], v1[1]); w.w = cvt_pk_bf16(v1[2], v1[3]); return w; }
; #define EPI_ROWLOOP for (int ai = 0; ai < 2; ++ai) _Pragma("unroll") for (int m = 0; m < 4; ++m)
;     __device__ __forceinline__ void operator()(const f32x4 (&acc)[2][2][4][2], const pg8::Unit& u, int wr, int wc, int fr, int fq) const {
;         const int row0 = u.pm * 256 + wr * 64 + fr, c0 = u.pn * 256 + wc * 32 + 8 * fq;
; #pragma unroll
;         EPI_ROWLOOP { const size_t ro = (size_t)(row0 + ai * 128 + m * 16) * 1024 + c0;
; #pragma unroll
;             for (int bj = 0; bj < 2; ++bj) {
;                 f32x4 r0, r1;
;                 if (resf) { r0 = *(const f32x4*)(resf + ro + bj * 128); r1 = *(const f32x4*)(resf + ro + bj * 128 + 4); }
;                 else { const u32x4 xv = *(const u32x4*)(resb + ro + bj * 128);
;                     r0[0] = __uint_as_float(xv.x << 16); r0[1] = __uint_as_float(xv.x & 0xffff0000u); r0[2] = __uint_as_float(xv.y << 16); r0[3] = __uint_as_float(xv.y & 0xffff0000u);
;                     r1[0] = __uint_as_float(xv.z << 16); r1[1] = __uint_as_float(xv.z & 0xffff0000u); r1[2] = __uint_as_float(xv.w << 16); r1[3] = __uint_as_float(xv.w & 0xffff0000u); }
;                 *(u32x4*)(Y + ro + bj * 128) = pack8(acc[ai][bj][m][0] * sc + r0 * ALPHA, acc[ai][bj][m][1] * sc + r1 * ALPHA);
;             } }
.LBB0_412:
	v_lshl_add_u32 v154, s58, 8, v139
	v_lshl_or_b32 v156, s61, 8, v140
	v_ashrrev_i32_e32 v155, 31, v154
	v_ashrrev_i32_e32 v157, 31, v156
	v_lshlrev_b64 v[134:135], 10, v[154:155]
	v_lshl_add_u64 v[134:135], v[134:135], 0, v[156:157]
	v_lshl_add_u64 v[158:159], v[134:135], 2, s[2:3]
	v_lshl_add_u64 v[160:161], v[134:135], 1, s[8:9]
	s_andn2_b64 vcc, exec, s[4:5]
	s_mov_b64 s[4:5], -1
	global_load_dwordx4 v[146:149], v[158:159], off
	s_nop 0
	global_load_dwordx4 v[150:153], v[158:159], off offset:16
	global_load_dwordx4 v[162:165], v[158:159], off offset:512
	s_nop 0
	global_load_dwordx4 v[166:169], v[158:159], off offset:528
	s_mov_b64 s[98:99], 0x10000
	v_lshl_add_u64 v[250:251], v[158:159], 0, s[98:99]
	global_load_dwordx4 v[170:173], v[250:251], off
	s_nop 0
	global_load_dwordx4 v[174:177], v[250:251], off offset:16
	global_load_dwordx4 v[178:181], v[250:251], off offset:512
	s_nop 0
	global_load_dwordx4 v[182:185], v[250:251], off offset:528
	s_mov_b64 s[98:99], 0x20000
	v_lshl_add_u64 v[250:251], v[158:159], 0, s[98:99]
	global_load_dwordx4 v[186:189], v[250:251], off
	s_nop 0
	global_load_dwordx4 v[190:193], v[250:251], off offset:16
	global_load_dwordx4 v[194:197], v[250:251], off offset:512
	s_nop 0
	global_load_dwordx4 v[198:201], v[250:251], off offset:528
	s_mov_b64 s[98:99], 0x30000
	v_lshl_add_u64 v[250:251], v[158:159], 0, s[98:99]
	global_load_dwordx4 v[202:205], v[250:251], off
	s_nop 0
	global_load_dwordx4 v[206:209], v[250:251], off offset:16
	global_load_dwordx4 v[226:229], v[250:251], off offset:512
	s_nop 0
	global_load_dwordx4 v[230:233], v[250:251], off offset:528
	s_mov_b64 s[98:99], 0x80000
	v_lshl_add_u64 v[250:251], v[158:159], 0, s[98:99]
	global_load_dwordx4 v[234:237], v[250:251], off
	s_nop 0
	global_load_dwordx4 v[238:241], v[250:251], off offset:16
	global_load_dwordx4 v[242:245], v[250:251], off offset:512
	s_nop 0
	global_load_dwordx4 v[246:249], v[250:251], off offset:528
	s_mov_b64 s[98:99], 0x90000
	v_lshl_add_u64 v[250:251], v[158:159], 0, s[98:99]
	global_load_dwordx4 v[210:213], v[250:251], off
	s_nop 0
	global_load_dwordx4 v[214:217], v[250:251], off offset:16
	global_load_dwordx4 v[218:221], v[250:251], off offset:512
	s_nop 0
	global_load_dwordx4 v[222:225], v[250:251], off offset:528
	s_waitcnt vmcnt(22)
	v_pk_fma_f32 v[128:129], v[148:149], s[12:13], v[128:129] op_sel_hi:[1,0,1]
	v_pk_fma_f32 v[126:127], v[146:147], s[12:13], v[126:127] op_sel_hi:[1,0,1]
	v_pk_fma_f32 v[146:147], v[152:153], s[12:13], v[124:125] op_sel_hi:[1,0,1]
	v_pk_fma_f32 v[124:125], v[150:151], s[12:13], v[122:123] op_sel_hi:[1,0,1]
	v_cvt_pk_bf16_f32 v122, v126, v127
	v_cvt_pk_bf16_f32 v123, v128, v129
	v_cvt_pk_bf16_f32 v124, v124, v125
	v_cvt_pk_bf16_f32 v125, v146, v147
	global_store_dwordx4 v[160:161], v[122:125], off
	s_mov_b64 s[98:99], 0xa0000
	v_lshl_add_u64 v[250:251], v[158:159], 0, s[98:99]
	global_load_dwordx4 v[122:125], v[250:251], off
	s_nop 0
	global_load_dwordx4 v[126:129], v[250:251], off offset:16
	s_waitcnt vmcnt(23)
	v_pk_fma_f32 v[120:121], v[164:165], s[12:13], v[120:121] op_sel_hi:[1,0,1]
	v_pk_fma_f32 v[118:119], v[162:163], s[12:13], v[118:119] op_sel_hi:[1,0,1]
	v_pk_fma_f32 v[162:163], v[168:169], s[12:13], v[116:117] op_sel_hi:[1,0,1]
	v_pk_fma_f32 v[116:117], v[166:167], s[12:13], v[114:115] op_sel_hi:[1,0,1]
	v_cvt_pk_bf16_f32 v114, v118, v119
	v_cvt_pk_bf16_f32 v115, v120, v121
	v_cvt_pk_bf16_f32 v116, v116, v117
	v_cvt_pk_bf16_f32 v117, v162, v163
	global_store_dwordx4 v[160:161], v[114:117], off offset:256
	global_load_dwordx4 v[114:117], v[250:251], off offset:512
	s_nop 0
	global_load_dwordx4 v[118:121], v[250:251], off offset:528
	s_waitcnt vmcnt(24)
	v_pk_fma_f32 v[112:113], v[172:173], s[12:13], v[112:113] op_sel_hi:[1,0,1]
	v_pk_fma_f32 v[110:111], v[170:171], s[12:13], v[110:111] op_sel_hi:[1,0,1]
	v_pk_fma_f32 v[170:171], v[176:177], s[12:13], v[108:109] op_sel_hi:[1,0,1]
	v_pk_fma_f32 v[108:109], v[174:175], s[12:13], v[106:107] op_sel_hi:[1,0,1]
	v_cvt_pk_bf16_f32 v106, v110, v111
	v_cvt_pk_bf16_f32 v107, v112, v113
	v_cvt_pk_bf16_f32 v108, v108, v109
	v_cvt_pk_bf16_f32 v109, v170, v171
	s_mov_b64 s[98:99], 0x8000
	v_lshl_add_u64 v[254:255], v[160:161], 0, s[98:99]
	global_store_dwordx4 v[254:255], v[106:109], off
	s_mov_b64 s[98:99], 0xb0000
	v_lshl_add_u64 v[250:251], v[158:159], 0, s[98:99]
	global_load_dwordx4 v[106:109], v[250:251], off
	s_nop 0
	global_load_dwordx4 v[110:113], v[250:251], off offset:16
	s_waitcnt vmcnt(25)
	v_pk_fma_f32 v[104:105], v[180:181], s[12:13], v[104:105] op_sel_hi:[1,0,1]
	v_pk_fma_f32 v[102:103], v[178:179], s[12:13], v[102:103] op_sel_hi:[1,0,1]
	v_pk_fma_f32 v[178:179], v[184:185], s[12:13], v[100:101] op_sel_hi:[1,0,1]
	v_pk_fma_f32 v[100:101], v[182:183], s[12:13], v[98:99] op_sel_hi:[1,0,1]
	v_cvt_pk_bf16_f32 v98, v102, v103
	v_cvt_pk_bf16_f32 v99, v104, v105
	v_cvt_pk_bf16_f32 v100, v100, v101
	v_cvt_pk_bf16_f32 v101, v178, v179
	global_store_dwordx4 v[254:255], v[98:101], off offset:256
	global_load_dwordx4 v[98:101], v[250:251], off offset:512
	s_nop 0
	global_load_dwordx4 v[102:105], v[250:251], off offset:528
	s_waitcnt vmcnt(26)
	v_pk_fma_f32 v[96:97], v[188:189], s[12:13], v[96:97] op_sel_hi:[1,0,1]
	v_pk_fma_f32 v[94:95], v[186:187], s[12:13], v[94:95] op_sel_hi:[1,0,1]
	v_pk_fma_f32 v[186:187], v[192:193], s[12:13], v[92:93] op_sel_hi:[1,0,1]
	v_pk_fma_f32 v[92:93], v[190:191], s[12:13], v[90:91] op_sel_hi:[1,0,1]
	v_cvt_pk_bf16_f32 v90, v94, v95
	v_cvt_pk_bf16_f32 v91, v96, v97
	v_cvt_pk_bf16_f32 v92, v92, v93
	v_cvt_pk_bf16_f32 v93, v186, v187
	s_mov_b64 s[98:99], 0x10000
	v_lshl_add_u64 v[254:255], v[160:161], 0, s[98:99]
	global_store_dwordx4 v[254:255], v[90:93], off
	s_waitcnt vmcnt(25)
; __device__ __forceinline__ u32x4 pack8(const f32x4 v0, const f32x4 v1) { u32x4 w; w.x = cvt_pk_bf16(v0[0], v0[1]); w.y = cvt_pk_bf16(v0[2], v0[3]); w.z = cvt_pk_bf16(v1[0], v1[1]); w.w = cvt_pk_bf16(v1[2], v1[3]); return w; }
; #define EPI_ROWLOOP for (int ai = 0; ai < 2; ++ai) _Pragma("unroll") for (int m = 0; m < 4; ++m)
;     __device__ __forceinline__ void operator()(const f32x4 (&acc)[2][2][4][2], const pg8::Unit& u, int wr, int wc, int fr, int fq) const {
;         const int row0 = u.pm * 256 + wr * 64 + fr, c0 = u.pn * 256 + wc * 32 + 8 * fq;
; #pragma unroll
;         EPI_ROWLOOP { const size_t ro = (size_t)(row0 + ai * 128 + m * 16) * 1024 + c0;
; #pragma unroll
;             for (int bj = 0; bj < 2; ++bj) {
;                 f32x4 r0, r1;
;                 if (resf) { r0 = *(const f32x4*)(resf + ro + bj * 128); r1 = *(const f32x4*)(resf + ro + bj * 128 + 4); }
;                 else { const u32x4 xv = *(const u32x4*)(resb + ro + bj * 128);
;                     r0[0] = __uint_as_float(xv.x << 16); r0[1] = __uint_as_float(xv.x & 0xffff0000u); r0[2] = __uint_as_float(xv.y << 16); r0[3] = __uint_as_float(xv.y & 0xffff0000u);
;                     r1[0] = __uint_as_float(xv.z << 16); r1[1] = __uint_as_float(xv.z & 0xffff0000u); r1[2] = __uint_as_float(xv.w << 16); r1[3] = __uint_as_float(xv.w & 0xffff0000u); }
;                 *(u32x4*)(Y + ro + bj * 128) = pack8(acc[ai][bj][m][0] * sc + r0 * ALPHA, acc[ai][bj][m][1] * sc + r1 * ALPHA);
;             } }
	v_pk_fma_f32 v[88:89], v[196:197], s[12:13], v[88:89] op_sel_hi:[1,0,1]
	v_pk_fma_f32 v[86:87], v[194:195], s[12:13], v[86:87] op_sel_hi:[1,0,1]
	v_pk_fma_f32 v[194:195], v[200:201], s[12:13], v[84:85] op_sel_hi:[1,0,1]
	v_pk_fma_f32 v[84:85], v[198:199], s[12:13], v[82:83] op_sel_hi:[1,0,1]
	v_cvt_pk_bf16_f32 v82, v86, v87
	v_cvt_pk_bf16_f32 v83, v88, v89
	v_cvt_pk_bf16_f32 v84, v84, v85
	v_cvt_pk_bf16_f32 v85, v194, v195
	global_store_dwordx4 v[254:255], v[82:85], off offset:256
	s_waitcnt vmcnt(24)
	v_pk_fma_f32 v[80:81], v[204:205], s[12:13], v[80:81] op_sel_hi:[1,0,1]
	v_pk_fma_f32 v[78:79], v[202:203], s[12:13], v[78:79] op_sel_hi:[1,0,1]
	v_pk_fma_f32 v[202:203], v[208:209], s[12:13], v[76:77] op_sel_hi:[1,0,1]
	v_pk_fma_f32 v[76:77], v[206:207], s[12:13], v[74:75] op_sel_hi:[1,0,1]
	v_cvt_pk_bf16_f32 v74, v78, v79
	v_cvt_pk_bf16_f32 v75, v80, v81
	v_cvt_pk_bf16_f32 v76, v76, v77
	v_cvt_pk_bf16_f32 v77, v202, v203
	s_mov_b64 s[98:99], 0x18000
	v_lshl_add_u64 v[254:255], v[160:161], 0, s[98:99]
	global_store_dwordx4 v[254:255], v[74:77], off
	s_waitcnt vmcnt(23)
	v_pk_fma_f32 v[72:73], v[228:229], s[12:13], v[72:73] op_sel_hi:[1,0,1]
	v_pk_fma_f32 v[70:71], v[226:227], s[12:13], v[70:71] op_sel_hi:[1,0,1]
	v_pk_fma_f32 v[226:227], v[232:233], s[12:13], v[68:69] op_sel_hi:[1,0,1]
	v_pk_fma_f32 v[68:69], v[230:231], s[12:13], v[66:67] op_sel_hi:[1,0,1]
	v_cvt_pk_bf16_f32 v66, v70, v71
	v_cvt_pk_bf16_f32 v67, v72, v73
	v_cvt_pk_bf16_f32 v68, v68, v69
	v_cvt_pk_bf16_f32 v69, v226, v227
	global_store_dwordx4 v[254:255], v[66:69], off offset:256
	s_waitcnt vmcnt(22)
	v_pk_fma_f32 v[64:65], v[236:237], s[12:13], v[64:65] op_sel_hi:[1,0,1]
	v_pk_fma_f32 v[62:63], v[234:235], s[12:13], v[62:63] op_sel_hi:[1,0,1]
	v_pk_fma_f32 v[234:235], v[240:241], s[12:13], v[60:61] op_sel_hi:[1,0,1]
	v_pk_fma_f32 v[60:61], v[238:239], s[12:13], v[58:59] op_sel_hi:[1,0,1]
	v_cvt_pk_bf16_f32 v58, v62, v63
	v_cvt_pk_bf16_f32 v59, v64, v65
	v_cvt_pk_bf16_f32 v60, v60, v61
	v_cvt_pk_bf16_f32 v61, v234, v235
	s_mov_b64 s[98:99], 0x40000
	v_lshl_add_u64 v[254:255], v[160:161], 0, s[98:99]
	global_store_dwordx4 v[254:255], v[58:61], off
	s_waitcnt vmcnt(21)
	v_pk_fma_f32 v[56:57], v[244:245], s[12:13], v[56:57] op_sel_hi:[1,0,1]
	v_pk_fma_f32 v[54:55], v[242:243], s[12:13], v[54:55] op_sel_hi:[1,0,1]
	v_pk_fma_f32 v[242:243], v[248:249], s[12:13], v[52:53] op_sel_hi:[1,0,1]
	v_pk_fma_f32 v[52:53], v[246:247], s[12:13], v[50:51] op_sel_hi:[1,0,1]
	v_cvt_pk_bf16_f32 v50, v54, v55
	v_cvt_pk_bf16_f32 v51, v56, v57
	v_cvt_pk_bf16_f32 v52, v52, v53
	v_cvt_pk_bf16_f32 v53, v242, v243
	global_store_dwordx4 v[254:255], v[50:53], off offset:256
	s_waitcnt vmcnt(20)
	v_pk_fma_f32 v[48:49], v[212:213], s[12:13], v[48:49] op_sel_hi:[1,0,1]
	v_pk_fma_f32 v[46:47], v[210:211], s[12:13], v[46:47] op_sel_hi:[1,0,1]
	v_pk_fma_f32 v[210:211], v[216:217], s[12:13], v[44:45] op_sel_hi:[1,0,1]
	v_pk_fma_f32 v[44:45], v[214:215], s[12:13], v[42:43] op_sel_hi:[1,0,1]
	v_cvt_pk_bf16_f32 v42, v46, v47
	v_cvt_pk_bf16_f32 v43, v48, v49
	v_cvt_pk_bf16_f32 v44, v44, v45
	v_cvt_pk_bf16_f32 v45, v210, v211
	s_mov_b64 s[98:99], 0x48000
	v_lshl_add_u64 v[254:255], v[160:161], 0, s[98:99]
	global_store_dwordx4 v[254:255], v[42:45], off
	s_waitcnt vmcnt(19)
	v_pk_fma_f32 v[40:41], v[220:221], s[12:13], v[40:41] op_sel_hi:[1,0,1]
	v_pk_fma_f32 v[38:39], v[218:219], s[12:13], v[38:39] op_sel_hi:[1,0,1]
	v_pk_fma_f32 v[218:219], v[224:225], s[12:13], v[36:37] op_sel_hi:[1,0,1]
	v_pk_fma_f32 v[36:37], v[222:223], s[12:13], v[34:35] op_sel_hi:[1,0,1]
	v_cvt_pk_bf16_f32 v34, v38, v39
	v_cvt_pk_bf16_f32 v35, v40, v41
	v_cvt_pk_bf16_f32 v36, v36, v37
	v_cvt_pk_bf16_f32 v37, v218, v219
	global_store_dwordx4 v[254:255], v[34:37], off offset:256
	s_waitcnt vmcnt(17)
	v_pk_fma_f32 v[32:33], v[124:125], s[12:13], v[32:33] op_sel_hi:[1,0,1]
	v_pk_fma_f32 v[30:31], v[122:123], s[12:13], v[30:31] op_sel_hi:[1,0,1]
	v_pk_fma_f32 v[122:123], v[128:129], s[12:13], v[28:29] op_sel_hi:[1,0,1]
	v_pk_fma_f32 v[28:29], v[126:127], s[12:13], v[26:27] op_sel_hi:[1,0,1]
	v_cvt_pk_bf16_f32 v26, v30, v31
	v_cvt_pk_bf16_f32 v27, v32, v33
	v_cvt_pk_bf16_f32 v28, v28, v29
	v_cvt_pk_bf16_f32 v29, v122, v123
	s_mov_b64 s[98:99], 0x50000
	v_lshl_add_u64 v[254:255], v[160:161], 0, s[98:99]
	global_store_dwordx4 v[254:255], v[26:29], off
	s_waitcnt vmcnt(15)
	v_pk_fma_f32 v[24:25], v[116:117], s[12:13], v[24:25] op_sel_hi:[1,0,1]
	v_pk_fma_f32 v[22:23], v[114:115], s[12:13], v[22:23] op_sel_hi:[1,0,1]
	v_pk_fma_f32 v[114:115], v[120:121], s[12:13], v[20:21] op_sel_hi:[1,0,1]
	v_pk_fma_f32 v[20:21], v[118:119], s[12:13], v[18:19] op_sel_hi:[1,0,1]
	v_cvt_pk_bf16_f32 v18, v22, v23
	v_cvt_pk_bf16_f32 v19, v24, v25
	v_cvt_pk_bf16_f32 v20, v20, v21
	v_cvt_pk_bf16_f32 v21, v114, v115
	global_store_dwordx4 v[254:255], v[18:21], off offset:256
	s_waitcnt vmcnt(13)
	v_pk_fma_f32 v[16:17], v[108:109], s[12:13], v[16:17] op_sel_hi:[1,0,1]
	v_pk_fma_f32 v[14:15], v[106:107], s[12:13], v[14:15] op_sel_hi:[1,0,1]
	v_pk_fma_f32 v[106:107], v[112:113], s[12:13], v[12:13] op_sel_hi:[1,0,1]
	v_pk_fma_f32 v[12:13], v[110:111], s[12:13], v[10:11] op_sel_hi:[1,0,1]
	v_cvt_pk_bf16_f32 v10, v14, v15
	v_cvt_pk_bf16_f32 v11, v16, v17
	v_cvt_pk_bf16_f32 v12, v12, v13
	v_cvt_pk_bf16_f32 v13, v106, v107
	s_mov_b64 s[98:99], 0x58000
	v_lshl_add_u64 v[254:255], v[160:161], 0, s[98:99]
	global_store_dwordx4 v[254:255], v[10:13], off
	s_waitcnt vmcnt(11)
	v_pk_fma_f32 v[8:9], v[100:101], s[12:13], v[8:9] op_sel_hi:[1,0,1]
	v_pk_fma_f32 v[6:7], v[98:99], s[12:13], v[6:7] op_sel_hi:[1,0,1]
	v_pk_fma_f32 v[98:99], v[104:105], s[12:13], v[4:5] op_sel_hi:[1,0,1]
	v_pk_fma_f32 v[4:5], v[102:103], s[12:13], v[2:3] op_sel_hi:[1,0,1]
	v_cvt_pk_bf16_f32 v2, v6, v7
	v_cvt_pk_bf16_f32 v3, v8, v9
	v_cvt_pk_bf16_f32 v4, v4, v5
	v_cvt_pk_bf16_f32 v5, v98, v99
	global_store_dwordx4 v[254:255], v[2:5], off offset:256
	s_cbranch_vccnz .LBB0_401
	s_andn2_b64 vcc, exec, s[6:7]
	s_cbranch_vccnz .LBB0_400
	s_barrier
	s_branch .LBB0_400

; __global__ void __launch_bounds__(512, 2) fwd_kernel(Args a) {
	.amdhsa_kernel _Z10fwd_kernel4Args
		.amdhsa_group_segment_fixed_size 0
		.amdhsa_private_segment_fixed_size 0
		.amdhsa_kernarg_size 544
		.amdhsa_user_sgpr_count 2
		.amdhsa_user_sgpr_dispatch_ptr 0
		.amdhsa_user_sgpr_queue_ptr 0
		.amdhsa_user_sgpr_kernarg_segment_ptr 1
		.amdhsa_user_sgpr_dispatch_id 0
		.amdhsa_user_sgpr_kernarg_preload_length 0
		.amdhsa_user_sgpr_kernarg_preload_offset 0
		.amdhsa_user_sgpr_private_segment_size 0
		.amdhsa_uses_dynamic_stack 0
		.amdhsa_enable_private_segment 0
		.amdhsa_system_sgpr_workgroup_id_x 1
		.amdhsa_system_sgpr_workgroup_id_y 0
		.amdhsa_system_sgpr_workgroup_id_z 0
		.amdhsa_system_sgpr_workgroup_info 0
		.amdhsa_system_vgpr_workitem_id 0
		.amdhsa_next_free_vgpr 256
		.amdhsa_next_free_sgpr 102
		.amdhsa_accum_offset 256
		.amdhsa_reserve_vcc 1
		.amdhsa_float_round_mode_32 0
		.amdhsa_float_round_mode_16_64 0
		.amdhsa_float_denorm_mode_32 3
		.amdhsa_float_denorm_mode_16_64 3
		.amdhsa_dx10_clamp 1
		.amdhsa_ieee_mode 1
		.amdhsa_fp16_overflow 0
		.amdhsa_tg_split 0
		.amdhsa_exception_fp_ieee_invalid_op 0
		.amdhsa_exception_fp_denorm_src 0
		.amdhsa_exception_fp_ieee_div_zero 0
		.amdhsa_exception_fp_ieee_overflow 0
		.amdhsa_exception_fp_ieee_underflow 0
		.amdhsa_exception_fp_ieee_inexact 0
		.amdhsa_exception_int_div_zero 0
	.end_amdhsa_kernel

; __global__ void __launch_bounds__(512, 2) fwd_kernel(Args a) {
amdhsa.kernels:
  - .agpr_count:     0
    .args:
      - .offset:         0
        .size:           288
        .value_kind:     by_value
      - .offset:         288
        .size:           4
        .value_kind:     hidden_block_count_x
      - .offset:         292
        .size:           4
        .value_kind:     hidden_block_count_y
      - .offset:         296
        .size:           4
        .value_kind:     hidden_block_count_z
      - .offset:         300
        .size:           2
        .value_kind:     hidden_group_size_x
      - .offset:         302
        .size:           2
        .value_kind:     hidden_group_size_y
      - .offset:         304
        .size:           2
        .value_kind:     hidden_group_size_z
      - .offset:         306
        .size:           2
        .value_kind:     hidden_remainder_x
      - .offset:         308
        .size:           2
        .value_kind:     hidden_remainder_y
      - .offset:         310
        .size:           2
        .value_kind:     hidden_remainder_z
      - .offset:         328
        .size:           8
        .value_kind:     hidden_global_offset_x
      - .offset:         336
        .size:           8
        .value_kind:     hidden_global_offset_y
      - .offset:         344
        .size:           8
        .value_kind:     hidden_global_offset_z
      - .offset:         352
        .size:           2
        .value_kind:     hidden_grid_dims
      - .offset:         408
        .size:           4
        .value_kind:     hidden_dynamic_lds_size
    .group_segment_fixed_size: 0
    .kernarg_segment_align: 8
    .kernarg_segment_size: 544
    .language:       OpenCL C
    .language_version:
      - 2
      - 0
    .max_flat_workgroup_size: 512
    .name:           _Z10fwd_kernel4Args
    .private_segment_fixed_size: 0
    .sgpr_count:     108
    .sgpr_spill_count: 129
    .symbol:         _Z10fwd_kernel4Args.kd
    .uniform_work_group_size: 1
    .uses_dynamic_stack: false
    .vgpr_count:     256
    .vgpr_spill_count: 0
    .wavefront_size: 64
